# final norm: output stores and residual / y16 / expert-row loads non-temporal
# speedup vs baseline: 1.0048x; 1.0048x over previous
.LBB0_1555:
	s_or_b64 exec, exec, s[8:9]
	s_lshl_b32 s22, s17, 11
	s_addk_i32 s22, 0x800
	s_min_i32 s23, s22, s0
	v_add_u32_e32 v29, s16, v23
	s_lshl_b32 s24, s17, 8
	v_cmp_gt_i32_e64 s[8:9], s23, v29
	s_waitcnt vmcnt(0)
	ds_write_b128 v67, v[0:3]
	s_waitcnt lgkmcnt(0)
	s_barrier
	s_and_saveexec_b64 s[10:11], s[8:9]
	s_cbranch_execz .LBB0_1557
	v_add_u32_e32 v0, s24, v29
	v_ashrrev_i32_e32 v1, 31, v0
	v_lshlrev_b64 v[2:3], 11, v[0:1]
	v_lshl_add_u64 v[2:3], v[20:21], 0, v[2:3]
	v_lshlrev_b64 v[0:1], 6, v[0:1]
	global_load_dwordx2 v[50:51], v[2:3], off nt
	global_load_dwordx2 v[52:53], v[2:3], off offset:512 nt
	global_load_dwordx2 v[56:57], v[2:3], off offset:1024 nt
	global_load_dwordx2 v[58:59], v[2:3], off offset:1536 nt
	v_lshl_or_b32 v0, v22, 2, v0
	v_lshl_add_u64 v[2:3], s[14:15], 0, v[0:1]
	v_lshl_add_u64 v[0:1], s[12:13], 0, v[0:1]
	global_load_dword v71, v[2:3], off
	global_load_dword v72, v[0:1], off

.LBB0_1579:
	v_add_u32_e32 v29, 8, v32
	v_cmp_gt_i32_e64 s[10:11], s23, v29
	v_cmp_le_i32_e64 s[8:9], s23, v29
	v_mov_b64_e32 v[50:51], v[48:49]
	v_mov_b64_e32 v[52:53], v[46:47]
	v_mov_b64_e32 v[56:57], v[44:45]
	v_mov_b64_e32 v[58:59], v[42:43]
	s_and_saveexec_b64 s[20:21], s[10:11]
	s_cbranch_execz .LBB0_1559
	v_add_u32_e32 v54, 8, v54
	v_ashrrev_i32_e32 v55, 31, v54
	v_lshlrev_b64 v[50:51], 11, v[54:55]
	v_lshl_add_u64 v[72:73], v[20:21], 0, v[50:51]
	v_lshlrev_b64 v[54:55], 6, v[54:55]
	global_load_dwordx2 v[50:51], v[72:73], off nt
	global_load_dwordx2 v[52:53], v[72:73], off offset:512 nt
	global_load_dwordx2 v[56:57], v[72:73], off offset:1024 nt
	global_load_dwordx2 v[58:59], v[72:73], off offset:1536 nt
	v_lshl_or_b32 v54, v22, 2, v54
	v_lshl_add_u64 v[74:75], s[14:15], 0, v[54:55]
	v_lshl_add_u64 v[54:55], s[12:13], 0, v[54:55]
	global_load_dword v71, v[74:75], off
	global_load_dword v72, v[54:55], off
	s_branch .LBB0_1559
